# P0-P1 barrier: two x rows per wave loaded while waiting at the barrier (second row consumed by the loop's second iteration)
# baseline (speedup 1.0000x reference)
.LBB0_73:
	s_or_b64 exec, exec, s[2:3]
	v_lshlrev_b32_e32 v132, 4, v178
	v_and_b32_e32 v134, 0x3f0, v132
	v_add_u32_e32 v135, 0x1000, v134
	global_load_dwordx4 v[2:5], v134, s[12:13]
	global_load_dwordx4 v[6:9], v134, s[12:13] offset:1024
	global_load_dwordx4 v[10:13], v134, s[12:13] offset:2048
	global_load_dwordx4 v[14:17], v134, s[12:13] offset:3072
	global_load_dwordx4 v[18:21], v135, s[12:13]
	global_load_dwordx4 v[22:25], v135, s[12:13] offset:1024
	global_load_dwordx4 v[26:29], v135, s[12:13] offset:2048
	global_load_dwordx4 v[30:33], v135, s[12:13] offset:3072
	v_lshrrev_b32_e32 v132, 6, v178
	v_lshl_add_u32 v132, s33, 3, v132
	v_mov_b32_e32 v133, 0
	v_lshlrev_b64 v[132:133], 13, v[132:133]
	v_lshl_add_u64 v[132:133], s[8:9], 0, v[132:133]
	v_mov_b32_e32 v135, 0
	v_lshl_add_u64 v[132:133], v[132:133], 0, v[134:135]
	s_mov_b64 s[100:101], 0x1000
	v_lshl_add_u64 v[132:133], v[132:133], 0, s[100:101]
	global_load_dwordx4 v[100:103], v[132:133], off
	global_load_dwordx4 v[104:107], v[132:133], off offset:1024
	global_load_dwordx4 v[108:111], v[132:133], off offset:2048
	global_load_dwordx4 v[112:115], v[132:133], off offset:3072
	global_load_dwordx4 v[116:119], v[132:133], off offset:-4096
	global_load_dwordx4 v[120:123], v[132:133], off offset:-3072
	global_load_dwordx4 v[124:127], v[132:133], off offset:-2048
	global_load_dwordx4 v[128:131], v[132:133], off offset:-1024
	s_mov_b64 s[100:101], 0x1000000
	v_lshl_add_u64 v[200:201], v[132:133], 0, s[100:101]
	global_load_dwordx4 v[180:183], v[200:201], off
	global_load_dwordx4 v[184:187], v[200:201], off offset:1024
	global_load_dwordx4 v[188:191], v[200:201], off offset:2048
	global_load_dwordx4 v[192:195], v[200:201], off offset:3072
	global_load_dwordx4 v[196:199], v[200:201], off offset:-4096
	global_load_dwordx4 v[236:239], v[200:201], off offset:-3072
	global_load_dwordx4 v[240:243], v[200:201], off offset:-2048
	global_load_dwordx4 v[244:247], v[200:201], off offset:-1024
	s_barrier
.LBB0_74:
	s_cmp_lt_i32 s94, 2
	s_cselect_b64 s[2:3], -1, 0
	s_and_b64 s[0:1], s[2:3], s[0:1]
	s_andn2_b64 vcc, exec, s[0:1]
	v_lshrrev_b32_e32 v179, 6, v178
	s_cbranch_vccnz .LBB0_79
	v_lshl_add_u32 v66, s33, 3, v179
	s_waitcnt lgkmcnt(0)
	s_movk_i32 s16, 0x2000
	v_cmp_gt_i32_e32 vcc, s16, v66
	s_and_saveexec_b64 s[2:3], vcc
	s_cbranch_execz .LBB0_78
	v_lshlrev_b32_e32 v1, 4, v178
	v_and_b32_e32 v34, 0x3f0, v1
	v_mov_b32_e32 v35, 0
	s_movk_i32 s17, 0x1000
	v_mbcnt_lo_u32_b32 v1, -1, 0
	v_lshl_add_u64 v[68:69], s[92:93], 0, v[34:35]
	v_mbcnt_hi_u32_b32 v34, -1, v1
	v_and_b32_e32 v1, 64, v34
	v_add_u32_e32 v35, 64, v1
	v_xor_b32_e32 v1, 32, v34
	v_cmp_lt_i32_e32 vcc, v1, v35
	v_xor_b32_e32 v36, 16, v34
	v_ashrrev_i32_e32 v67, 31, v66
	v_cndmask_b32_e32 v1, v34, v1, vcc
	v_cmp_lt_i32_e32 vcc, v36, v35
	s_mov_b64 s[6:7], 0x1000
	s_lshl_b32 s4, s96, 3
	v_cndmask_b32_e32 v36, v34, v36, vcc
	v_lshlrev_b32_e32 v74, 2, v36
	v_xor_b32_e32 v36, 8, v34
	v_cmp_lt_i32_e32 vcc, v36, v35
	s_ashr_i32 s5, s4, 31
	s_mov_b64 s[10:11], 0x40000
	v_cndmask_b32_e32 v36, v34, v36, vcc
	v_lshlrev_b32_e32 v75, 2, v36
	v_xor_b32_e32 v36, 4, v34
	v_cmp_lt_i32_e32 vcc, v36, v35
	v_lshlrev_b32_e32 v1, 2, v1
	s_mov_b64 s[12:13], 0
	v_cndmask_b32_e32 v36, v34, v36, vcc
	v_lshlrev_b32_e32 v76, 2, v36
	v_xor_b32_e32 v36, 2, v34
	v_cmp_lt_i32_e32 vcc, v36, v35
	s_mov_b32 s18, 0x800000
	s_movk_i32 s19, 0x1fff
	v_cndmask_b32_e32 v36, v34, v36, vcc
	v_lshlrev_b32_e32 v77, 2, v36
	v_xor_b32_e32 v36, 1, v34
	v_cmp_lt_i32_e32 vcc, v36, v35
	s_nop 1
	v_cndmask_b32_e32 v34, v34, v36, vcc
	v_lshlrev_b32_e32 v78, 2, v34
	v_lshlrev_b64 v[34:35], 13, v[66:67]
	v_and_b32_e32 v36, 63, v178
	v_lshl_or_b32 v34, v36, 4, v34
	v_lshl_add_u64 v[34:35], s[8:9], 0, v[34:35]
	v_lshl_add_u64 v[70:71], v[34:35], 0, s[6:7]
	v_lshlrev_b64 v[34:35], 12, v[66:67]
	v_lshl_or_b32 v34, v36, 3, v34
	v_lshl_add_u64 v[34:35], s[90:91], 0, v[34:35]
	s_lshl_b64 s[6:7], s[4:5], 13
	v_lshl_add_u64 v[72:73], v[34:35], 0, s[10:11]
	s_lshl_b64 s[10:11], s[4:5], 12
	s_movk_i32 s5, 0x3000
	v_mov_b32_e32 v67, 0x358637bd
	s_waitcnt vmcnt(0)
	v_mov_b64_e32 v[38:39], v[100:101]
	v_mov_b64_e32 v[40:41], v[102:103]
	v_mov_b64_e32 v[34:35], v[104:105]
	v_mov_b64_e32 v[36:37], v[106:107]
	v_mov_b64_e32 v[46:47], v[108:109]
	v_mov_b64_e32 v[48:49], v[110:111]
	v_mov_b64_e32 v[42:43], v[112:113]
	v_mov_b64_e32 v[44:45], v[114:115]
	v_mov_b64_e32 v[50:51], v[116:117]
	v_mov_b64_e32 v[52:53], v[118:119]
	v_mov_b64_e32 v[54:55], v[120:121]
	v_mov_b64_e32 v[56:57], v[122:123]
	v_mov_b64_e32 v[62:63], v[124:125]
	v_mov_b64_e32 v[64:65], v[126:127]
	v_mov_b64_e32 v[58:59], v[128:129]
	v_mov_b64_e32 v[60:61], v[130:131]
	s_mov_b32 s99, 0
	s_branch .Lp1_have_row
.Lp1_row1:
	s_mov_b32 s99, 1
	v_mov_b64_e32 v[38:39], v[180:181]
	v_mov_b64_e32 v[40:41], v[182:183]
	v_mov_b64_e32 v[34:35], v[184:185]
	v_mov_b64_e32 v[36:37], v[186:187]
	v_mov_b64_e32 v[46:47], v[188:189]
	v_mov_b64_e32 v[48:49], v[190:191]
	v_mov_b64_e32 v[42:43], v[192:193]
	v_mov_b64_e32 v[44:45], v[194:195]
	v_mov_b64_e32 v[50:51], v[196:197]
	v_mov_b64_e32 v[52:53], v[198:199]
	v_mov_b64_e32 v[54:55], v[236:237]
	v_mov_b64_e32 v[56:57], v[238:239]
	v_mov_b64_e32 v[62:63], v[240:241]
	v_mov_b64_e32 v[64:65], v[242:243]
	v_mov_b64_e32 v[58:59], v[244:245]
	v_mov_b64_e32 v[60:61], v[246:247]
	s_branch .Lp1_have_row
.LBB0_77:
	s_cmp_eq_u32 s99, 0
	s_cbranch_scc1 .Lp1_row1
	global_load_dwordx4 v[38:41], v[70:71], off
	global_load_dwordx4 v[34:37], v[70:71], off offset:1024
	global_load_dwordx4 v[46:49], v[70:71], off offset:2048
	global_load_dwordx4 v[42:45], v[70:71], off offset:3072
	global_load_dwordx4 v[50:53], v[70:71], off offset:-4096
	global_load_dwordx4 v[54:57], v[70:71], off offset:-3072
	global_load_dwordx4 v[62:65], v[70:71], off offset:-2048
	global_load_dwordx4 v[58:61], v[70:71], off offset:-1024
